# attention QK: counted LDS waits grouped per 4 MFMAs (fewer issue slots)
# speedup vs baseline: 1.0092x; 1.0033x over previous
.LBB0_1173:
	s_mul_hi_u32 s7, s80, 0xaaaaaaab
	s_lshr_b32 s7, s7, 1
	s_mul_i32 s7, s7, 0xfffee000
	s_add_i32 s7, s7, 0
	v_add_u32_e32 v166, s6, v159
	v_add_u32_e32 v167, s6, v161
	v_add_u32_e32 v185, s6, v162
	v_add_u32_e32 v230, s6, v163
	ds_read_b128 v[66:69], v166 offset:32768
	ds_read_b128 v[82:85], v167 offset:32768
	ds_read_b128 v[86:89], v185 offset:32768
	ds_read_b128 v[90:93], v230 offset:32768
	ds_read_b128 v[94:97], v166 offset:32896
	ds_read_b128 v[186:189], v167 offset:32896
	ds_read_b128 v[190:193], v185 offset:32896
	ds_read_b128 v[194:197], v230 offset:32896
	ds_read_b128 v[198:201], v158
	ds_read_b128 v[202:205], v166 offset:33024
	ds_read_b128 v[206:209], v158 offset:1024
	ds_read_b128 v[210:213], v167 offset:33024
	ds_read_b128 v[214:217], v158 offset:2048
	ds_read_b128 v[218:221], v185 offset:33024
	ds_read_b128 v[222:225], v158 offset:3072
	s_waitcnt lgkmcnt(14)
	v_mfma_f32_32x32x16_bf16 v[66:81], v[66:69], v[126:129], 0
	ds_read_b128 v[226:229], v230 offset:33024
	s_waitcnt lgkmcnt(14)
	v_mfma_f32_32x32x16_bf16 v[66:81], v[82:85], v[122:125], v[66:81]
	s_waitcnt lgkmcnt(13)
	v_mfma_f32_32x32x16_bf16 v[66:81], v[86:89], v[118:121], v[66:81]
	s_waitcnt lgkmcnt(12)
	v_mfma_f32_32x32x16_bf16 v[66:81], v[90:93], v[114:117], v[66:81]
	s_waitcnt lgkmcnt(11)
	v_mfma_f32_32x32x16_bf16 v[66:81], v[94:97], v[110:113], v[66:81]
	s_waitcnt lgkmcnt(8)
	v_mfma_f32_32x32x16_bf16 v[66:81], v[186:189], v[106:109], v[66:81]
	ds_read_b128 v[186:189], v166 offset:45056
	v_mfma_f32_32x32x16_bf16 v[66:81], v[190:193], v[102:105], v[66:81]
	ds_read_b128 v[190:193], v167 offset:45056
	v_mfma_f32_32x32x16_bf16 v[66:81], v[194:197], v[98:101], v[66:81]
	ds_read_b128 v[194:197], v185 offset:45056
	s_waitcnt lgkmcnt(3)
	v_mfma_f32_32x32x16_bf16 v[66:81], v[202:205], v[198:201], v[66:81]
	ds_read_b128 v[202:205], v230 offset:45056
	v_mfma_f32_32x32x16_bf16 v[66:81], v[210:213], v[206:209], v[66:81]
	ds_read_b128 v[210:213], v166 offset:45184
	v_mfma_f32_32x32x16_bf16 v[66:81], v[218:221], v[214:217], v[66:81]
	ds_read_b128 v[218:221], v167 offset:45184
	v_mfma_f32_32x32x16_bf16 v[66:81], v[226:229], v[222:225], v[66:81]
	ds_read_b128 v[226:229], v185 offset:45184
	s_waitcnt lgkmcnt(3)
	v_mfma_f32_32x32x16_bf16 v[82:97], v[186:189], v[126:129], 0
	ds_read_b128 v[186:189], v230 offset:45184
	s_add_i32 s6, s78, 1
	s_min_u32 s6, s6, s14
	v_mfma_f32_32x32x16_bf16 v[82:97], v[190:193], v[122:125], v[82:97]
	ds_read_b128 v[246:249], v166 offset:45312
	s_lshl_b32 s10, s6, 6
	v_mfma_f32_32x32x16_bf16 v[82:97], v[194:197], v[118:121], v[82:97]
	ds_read_b128 v[242:245], v167 offset:45312
	s_cmp_lt_u32 s6, 4
	s_cselect_b32 s6, s74, s15
	s_add_i32 s6, s6, s10
	v_mfma_f32_32x32x16_bf16 v[82:97], v[202:205], v[114:117], v[82:97]
	ds_read_b128 v[238:241], v185 offset:45312
	s_mul_hi_i32 s11, s6, 0x1080
	s_mulk_i32 s6, 0x1080
	s_waitcnt lgkmcnt(3)
	v_mfma_f32_32x32x16_bf16 v[82:97], v[210:213], v[110:113], v[82:97]
	ds_read_b128 v[234:237], v230 offset:45312
	s_add_u32 s10, s3, s6
	s_addc_u32 s11, s35, s11
	s_add_i32 s6, s7, s30
	v_mfma_f32_32x32x16_bf16 v[82:97], v[218:221], v[106:109], v[82:97]
	s_add_i32 s6, s6, s8
	s_add_i32 m0, s6, 0x1a000
	s_nop 0
	global_load_lds_dwordx4 v232, s[10:11]
	v_mfma_f32_32x32x16_bf16 v[82:97], v[226:229], v[102:105], v[82:97]
	s_add_i32 m0, s6, 0x1a400
	v_mfma_f32_32x32x16_bf16 v[82:97], v[186:189], v[98:101], v[82:97]
	global_load_lds_dwordx4 v251, s[10:11]
	s_add_i32 m0, s6, 0x1a800
	s_waitcnt lgkmcnt(0)
	v_mfma_f32_32x32x16_bf16 v[82:97], v[246:249], v[198:201], v[82:97]
	v_mfma_f32_32x32x16_bf16 v[82:97], v[242:245], v[206:209], v[82:97]
	global_load_lds_dwordx4 v252, s[10:11]
	v_mfma_f32_32x32x16_bf16 v[82:97], v[238:241], v[214:217], v[82:97]
	v_mfma_f32_32x32x16_bf16 v[82:97], v[234:237], v[222:225], v[82:97]
	v_exp_f32_e32 v194, v130
	v_add_f32_e32 v130, 0, v178
	v_add_f32_e32 v130, v182, v130
	v_add_f32_e32 v130, v179, v130
	v_add_f32_e32 v130, v183, v130
	v_add_f32_e32 v130, v180, v130
	v_add_f32_e32 v130, v184, v130
	v_add_f32_e32 v130, v177, v130
	v_add_f32_e32 v130, v181, v130
	v_add_f32_e32 v130, v171, v130
	v_add_f32_e32 v130, v175, v130
	v_add_f32_e32 v130, v172, v130
	v_add_f32_e32 v130, v176, v130
	v_exp_f32_e32 v146, v146
	v_add_f32_e32 v130, v168, v130
	v_exp_f32_e32 v147, v147
	v_add_f32_e32 v130, v173, v130
	v_exp_f32_e32 v167, v144
	v_add_f32_e32 v130, v169, v130
	v_exp_f32_e32 v185, v145
	v_add_f32_e32 v130, v174, v130
	v_exp_f32_e32 v186, v142
	v_add_f32_e32 v130, v146, v130
	v_exp_f32_e32 v187, v143
	v_add_f32_e32 v130, v147, v130
	v_exp_f32_e32 v188, v140
	v_add_f32_e32 v130, v167, v130
	v_exp_f32_e32 v189, v141
	v_add_f32_e32 v130, v185, v130
	v_exp_f32_e32 v190, v138
	v_add_f32_e32 v130, v186, v130
	v_exp_f32_e32 v191, v139
	v_add_f32_e32 v130, v187, v130
	v_exp_f32_e32 v192, v136
	v_add_f32_e32 v130, v188, v130
	v_exp_f32_e32 v193, v137
	v_add_f32_e32 v130, v189, v130
	v_exp_f32_e32 v132, v132
	v_add_f32_e32 v130, v190, v130
	v_exp_f32_e32 v133, v133
	v_add_f32_e32 v130, v191, v130
	v_add_f32_e32 v130, v192, v130
	v_exp_f32_e32 v195, v131
	v_add_f32_e32 v130, v193, v130
	v_add_f32_e32 v130, v132, v130
	v_add_f32_e32 v130, v133, v130
	v_add_f32_e32 v130, v194, v130
	v_add_f32_e32 v136, v195, v130
	v_mov_b32_e32 v137, v136
	v_cvt_pk_bf16_f32 v138, v178, v182
	v_cvt_pk_bf16_f32 v139, v179, v183
	v_cvt_pk_bf16_f32 v140, v180, v184
	v_cvt_pk_bf16_f32 v141, v177, v181
	v_cvt_pk_bf16_f32 v142, v171, v175
	v_cvt_pk_bf16_f32 v143, v172, v176
	v_cvt_pk_bf16_f32 v144, v168, v173
	v_cvt_pk_bf16_f32 v145, v169, v174
	v_cvt_pk_bf16_f32 v166, v146, v147
	v_cvt_pk_bf16_f32 v167, v167, v185
	v_cvt_pk_bf16_f32 v168, v186, v187
	v_cvt_pk_bf16_f32 v169, v188, v189
	s_nop 1
	v_permlane32_swap_b32_e32 v136, v137
	v_permlane32_swap_b32_e32 v138, v140
	v_permlane32_swap_b32_e32 v167, v169
	v_cvt_pk_bf16_f32 v130, v190, v191
	v_cvt_pk_bf16_f32 v131, v192, v193
	v_cvt_pk_bf16_f32 v132, v132, v133
	v_cvt_pk_bf16_f32 v133, v194, v195
	v_permlane32_swap_b32_e32 v139, v141
	v_permlane32_swap_b32_e32 v142, v144
	v_permlane32_swap_b32_e32 v143, v145
	v_permlane32_swap_b32_e32 v166, v168
	v_permlane32_swap_b32_e32 v130, v132
	v_permlane32_swap_b32_e32 v131, v133
	ds_read_b64_tr_b16 v[172:173], v160 offset:0
	ds_read_b64_tr_b16 v[174:175], v160 offset:0x800
	ds_read_b64_tr_b16 v[176:177], v160 offset:0x1000
	ds_read_b64_tr_b16 v[178:179], v160 offset:0x1800
	ds_read_b64_tr_b16 v[180:181], v160 offset:0x2000
	ds_read_b64_tr_b16 v[182:183], v160 offset:0x2800
	ds_read_b64_tr_b16 v[184:185], v160 offset:0x3000
	ds_read_b64_tr_b16 v[186:187], v160 offset:0x3800
	s_nop 0
	s_waitcnt lgkmcnt(6)
	v_mfma_f32_32x32x16_bf16 v[2:17], v[138:141], v[172:175], v[2:17]
	ds_read_b64_tr_b16 v[172:173], v160 offset:0x200
	ds_read_b64_tr_b16 v[174:175], v160 offset:0xa00
	s_waitcnt lgkmcnt(6)
	v_mfma_f32_32x32x16_bf16 v[2:17], v[142:145], v[176:179], v[2:17]
	ds_read_b64_tr_b16 v[176:177], v160 offset:0x1200
	ds_read_b64_tr_b16 v[178:179], v160 offset:0x1a00
	s_waitcnt lgkmcnt(6)
	v_mfma_f32_32x32x16_bf16 v[2:17], v[166:169], v[180:183], v[2:17]
	ds_read_b64_tr_b16 v[180:181], v160 offset:0x2200
	ds_read_b64_tr_b16 v[182:183], v160 offset:0x2a00
	ds_read_b64_tr_b16 v[188:189], v160 offset:0x3200
	ds_read_b64_tr_b16 v[190:191], v160 offset:0x3a00
	s_waitcnt lgkmcnt(8)
	v_mfma_f32_32x32x16_bf16 v[2:17], v[130:133], v[184:187], v[2:17]
	s_waitcnt lgkmcnt(6)
	v_mfma_f32_32x32x16_bf16 v[50:65], v[138:141], v[172:175], v[50:65]
	ds_read_b64_tr_b16 v[172:173], v160 offset:0x400
	ds_read_b64_tr_b16 v[174:175], v160 offset:0xc00
	s_waitcnt lgkmcnt(6)
	v_mfma_f32_32x32x16_bf16 v[50:65], v[142:145], v[176:179], v[50:65]
	ds_read_b64_tr_b16 v[176:177], v160 offset:0x1400
	ds_read_b64_tr_b16 v[178:179], v160 offset:0x1c00
	s_waitcnt lgkmcnt(6)
	v_mfma_f32_32x32x16_bf16 v[50:65], v[166:169], v[180:183], v[50:65]
	ds_read_b64_tr_b16 v[180:181], v160 offset:0x2400
	ds_read_b64_tr_b16 v[182:183], v160 offset:0x2c00
	ds_read_b64_tr_b16 v[184:185], v160 offset:0x3400
	ds_read_b64_tr_b16 v[186:187], v160 offset:0x3c00
	s_waitcnt lgkmcnt(8)
	v_mfma_f32_32x32x16_bf16 v[50:65], v[130:133], v[188:191], v[50:65]
	s_waitcnt lgkmcnt(6)
	v_mfma_f32_32x32x16_bf16 v[34:49], v[138:141], v[172:175], v[34:49]
	ds_read_b64_tr_b16 v[172:173], v160 offset:0x600
	ds_read_b64_tr_b16 v[174:175], v160 offset:0xe00
	s_waitcnt lgkmcnt(6)
	v_mfma_f32_32x32x16_bf16 v[34:49], v[142:145], v[176:179], v[34:49]
	ds_read_b64_tr_b16 v[176:177], v160 offset:0x1600
	ds_read_b64_tr_b16 v[178:179], v160 offset:0x1e00
	s_waitcnt lgkmcnt(6)
	v_mfma_f32_32x32x16_bf16 v[34:49], v[166:169], v[180:183], v[34:49]
	ds_read_b64_tr_b16 v[180:181], v160 offset:0x2600
	ds_read_b64_tr_b16 v[182:183], v160 offset:0x2e00
	ds_read_b64_tr_b16 v[188:189], v160 offset:0x3600
	ds_read_b64_tr_b16 v[190:191], v160 offset:0x3e00
	s_waitcnt lgkmcnt(8)
	v_mfma_f32_32x32x16_bf16 v[34:49], v[130:133], v[184:187], v[34:49]
	v_max_f32_e32 v146, v67, v67
	v_max_f32_e32 v147, v66, v66
	v_max_f32_e32 v146, v147, v146
	v_max3_f32 v146, v146, v68, v69
	v_max3_f32 v146, v146, v70, v71
	s_waitcnt lgkmcnt(6)
	v_mfma_f32_32x32x16_bf16 v[18:33], v[138:141], v[172:175], v[18:33]
	v_max3_f32 v138, v146, v72, v73
	v_max3_f32 v138, v138, v74, v75
	v_max3_f32 v138, v138, v76, v77
	v_max3_f32 v138, v138, v78, v79
	v_max3_f32 v138, v138, v80, v81
	v_max3_f32 v138, v138, v82, v83
	v_max3_f32 v138, v138, v84, v85
	v_max3_f32 v138, v138, v86, v87
	v_max3_f32 v138, v138, v88, v89
	v_max3_f32 v138, v138, v90, v91
	v_max3_f32 v138, v138, v92, v93
	v_max3_f32 v138, v138, v94, v95
	v_max3_f32 v138, v138, v96, v97
	v_mov_b32_e32 v139, v138
	s_nop 1
	v_permlane32_swap_b32_e32 v138, v139
	v_max_f32_e32 v139, v139, v139
	v_max_f32_e32 v138, v138, v138
	v_max_f32_e32 v138, v138, v139
	v_sub_f32_e32 v139, v138, v165
	s_waitcnt lgkmcnt(4)
	v_mfma_f32_32x32x16_bf16 v[18:33], v[142:145], v[176:179], v[18:33]
	v_cmp_ge_f32_e32 vcc, s65, v139
	s_waitcnt vmcnt(3) lgkmcnt(0)
	s_barrier
	s_cmp_eq_u64 vcc, exec
	s_cselect_b64 s[6:7], -1, 0
	s_cmp_lt_u32 s78, 4
	s_cselect_b32 s12, s74, s15
	s_add_i32 s12, s12, s9
	s_mul_hi_i32 s13, s12, 0x1080
	s_mulk_i32 s12, 0x1080
	s_add_u32 s12, s3, s12
	s_mov_b32 m0, s70
	s_addc_u32 s13, s35, s13
	global_load_lds_dwordx4 v253, s[12:13]
	s_mov_b32 m0, s72
	v_mfma_f32_32x32x16_bf16 v[18:33], v[166:169], v[180:183], v[18:33]
	global_load_lds_dwordx4 v254, s[12:13]
	v_max_f32_e32 v139, v165, v165
	v_max_f32_e32 v138, v139, v138
	v_sub_f32_e32 v139, v165, v138
	v_mul_f32_e32 v139, 0x3dd53b94, v139
	v_exp_f32_e32 v139, v139
	v_mfma_f32_32x32x16_bf16 v[18:33], v[130:133], v[188:191], v[18:33]
	v_cndmask_b32_e64 v167, v139, 1.0, s[6:7]
	v_cmp_gt_f32_e32 vcc, 1.0, v167
	s_cbranch_vccz .LBB0_1177
	s_and_saveexec_b64 s[12:13], s[4:5]
	ds_write_b32 v155, v167 offset:128
	s_or_b64 exec, exec, s[12:13]
	s_waitcnt lgkmcnt(0)
	v_add_u32_e32 v139, s69, v134
	ds_read_b128 v[130:133], v139 offset:224
	ds_read_b128 v[140:143], v139 offset:192
	ds_read_b128 v[144:147], v139 offset:160
	ds_read_b128 v[172:175], v139 offset:128
	s_waitcnt lgkmcnt(0)
	v_pk_mul_f32 v[14:15], v[14:15], v[130:131]
	v_pk_mul_f32 v[10:11], v[10:11], v[140:141]
	v_pk_mul_f32 v[6:7], v[6:7], v[144:145]
	v_pk_mul_f32 v[16:17], v[16:17], v[132:133]
	v_pk_mul_f32 v[12:13], v[12:13], v[142:143]
	v_pk_mul_f32 v[8:9], v[8:9], v[146:147]
	v_pk_mul_f32 v[4:5], v[4:5], v[174:175]
	v_pk_mul_f32 v[2:3], v[2:3], v[172:173]
	v_pk_mul_f32 v[62:63], v[62:63], v[130:131]
	v_pk_mul_f32 v[58:59], v[58:59], v[140:141]
	v_pk_mul_f32 v[54:55], v[54:55], v[144:145]
	v_pk_mul_f32 v[64:65], v[64:65], v[132:133]
	v_pk_mul_f32 v[60:61], v[60:61], v[142:143]
	v_pk_mul_f32 v[56:57], v[56:57], v[146:147]
	v_pk_mul_f32 v[52:53], v[52:53], v[174:175]
	v_pk_mul_f32 v[50:51], v[50:51], v[172:173]
	v_pk_mul_f32 v[46:47], v[46:47], v[130:131]
	v_pk_mul_f32 v[42:43], v[42:43], v[140:141]
	v_pk_mul_f32 v[38:39], v[38:39], v[144:145]
	v_pk_mul_f32 v[48:49], v[48:49], v[132:133]
	v_pk_mul_f32 v[44:45], v[44:45], v[142:143]
	v_pk_mul_f32 v[40:41], v[40:41], v[146:147]
	v_pk_mul_f32 v[36:37], v[36:37], v[174:175]
	v_pk_mul_f32 v[34:35], v[34:35], v[172:173]
	v_pk_mul_f32 v[30:31], v[30:31], v[130:131]
	v_pk_mul_f32 v[26:27], v[26:27], v[140:141]
	v_pk_mul_f32 v[22:23], v[22:23], v[144:145]
	v_pk_mul_f32 v[32:33], v[32:33], v[132:133]
	v_pk_mul_f32 v[28:29], v[28:29], v[142:143]
	v_pk_mul_f32 v[24:25], v[24:25], v[146:147]
	v_pk_mul_f32 v[20:21], v[20:21], v[174:175]
	v_pk_mul_f32 v[18:19], v[18:19], v[172:173]
.LBB0_1177:
	v_cndmask_b32_e64 v130, v138, v165, s[6:7]
	s_mul_hi_u32 s12, s79, 0xaaaaaaab
	v_mul_f32_e32 v131, 0xbdd53b94, v130
	s_lshr_b32 s12, s12, 1
	v_fmamk_f32 v66, v66, 0x3dd53b94, v131
	v_fmamk_f32 v68, v68, 0x3dd53b94, v131
	v_fmamk_f32 v70, v70, 0x3dd53b94, v131
	v_fmamk_f32 v72, v72, 0x3dd53b94, v131
	s_mul_i32 s12, s12, 0xfffee000
	v_fmamk_f32 v74, v74, 0x3dd53b94, v131
	v_fmamk_f32 v76, v76, 0x3dd53b94, v131
	v_fmamk_f32 v78, v78, 0x3dd53b94, v131
	v_fmamk_f32 v80, v80, 0x3dd53b94, v131
	v_fmamk_f32 v132, v82, 0x3dd53b94, v131
	v_fmamk_f32 v133, v84, 0x3dd53b94, v131
	v_fmamk_f32 v146, v86, 0x3dd53b94, v131
	v_fmamk_f32 v147, v88, 0x3dd53b94, v131
	v_fmamk_f32 v165, v90, 0x3dd53b94, v131
	v_fmamk_f32 v166, v92, 0x3dd53b94, v131
	v_fmamk_f32 v168, v94, 0x3dd53b94, v131
	v_fmamk_f32 v169, v96, 0x3dd53b94, v131
	v_exp_f32_e32 v171, v66
	v_exp_f32_e32 v224, v68
	v_exp_f32_e32 v225, v70
	v_exp_f32_e32 v226, v72
	v_fmamk_f32 v66, v67, 0x3dd53b94, v131
	v_fmamk_f32 v67, v69, 0x3dd53b94, v131
	v_fmamk_f32 v68, v71, 0x3dd53b94, v131
	v_fmamk_f32 v69, v73, 0x3dd53b94, v131
	v_fmamk_f32 v70, v75, 0x3dd53b94, v131
	v_fmamk_f32 v71, v77, 0x3dd53b94, v131
	v_fmamk_f32 v72, v79, 0x3dd53b94, v131
	v_fmamk_f32 v73, v81, 0x3dd53b94, v131
	v_fmamk_f32 v231, v83, 0x3dd53b94, v131
	v_fmamk_f32 v233, v85, 0x3dd53b94, v131
	v_fmamk_f32 v234, v87, 0x3dd53b94, v131
	v_fmamk_f32 v235, v89, 0x3dd53b94, v131
	v_fmamk_f32 v236, v91, 0x3dd53b94, v131
	v_fmamk_f32 v245, v93, 0x3dd53b94, v131
	v_fmamk_f32 v246, v95, 0x3dd53b94, v131
	v_fmac_f32_e32 v131, 0x3dd53b94, v97
	s_add_i32 s12, s12, 0
	v_exp_f32_e32 v227, v74
	v_exp_f32_e32 v228, v76
	v_exp_f32_e32 v229, v78
	v_exp_f32_e32 v230, v80
	v_exp_f32_e32 v237, v66
	v_exp_f32_e32 v238, v67
	v_exp_f32_e32 v239, v68
	v_exp_f32_e32 v240, v69
	v_exp_f32_e32 v241, v70
	v_exp_f32_e32 v242, v71
	v_exp_f32_e32 v243, v72
	v_exp_f32_e32 v244, v73
	v_add_u32_e32 v196, s16, v159
	v_add_u32_e32 v204, s16, v161
	v_add_u32_e32 v212, s16, v162
	v_add_u32_e32 v220, s16, v163
	ds_read_b128 v[66:69], v196 offset:32768
	ds_read_b128 v[82:85], v204 offset:32768
	ds_read_b128 v[86:89], v212 offset:32768
	ds_read_b128 v[90:93], v220 offset:32768
	ds_read_b128 v[94:97], v196 offset:32896
	ds_read_b128 v[138:141], v204 offset:32896
	ds_read_b128 v[142:145], v212 offset:32896
	ds_read_b128 v[172:175], v220 offset:32896
	ds_read_b128 v[176:179], v158
	ds_read_b128 v[180:183], v196 offset:33024
	ds_read_b128 v[184:187], v158 offset:1024
	ds_read_b128 v[188:191], v204 offset:33024
	ds_read_b128 v[192:195], v158 offset:2048
	ds_read_b128 v[200:203], v212 offset:33024
	ds_read_b128 v[208:211], v158 offset:3072
	s_waitcnt lgkmcnt(14)
	v_mfma_f32_32x32x16_bf16 v[66:81], v[66:69], v[126:129], 0
	ds_read_b128 v[216:219], v220 offset:33024
	s_waitcnt lgkmcnt(14)
	v_mfma_f32_32x32x16_bf16 v[66:81], v[82:85], v[122:125], v[66:81]
	s_waitcnt lgkmcnt(13)
	v_mfma_f32_32x32x16_bf16 v[66:81], v[86:89], v[118:121], v[66:81]
	s_waitcnt lgkmcnt(12)
	v_mfma_f32_32x32x16_bf16 v[66:81], v[90:93], v[114:117], v[66:81]
	s_waitcnt lgkmcnt(11)
	v_mfma_f32_32x32x16_bf16 v[66:81], v[94:97], v[110:113], v[66:81]
	s_waitcnt lgkmcnt(8)
	v_mfma_f32_32x32x16_bf16 v[66:81], v[138:141], v[106:109], v[66:81]
	ds_read_b128 v[138:141], v196 offset:45056
	v_mfma_f32_32x32x16_bf16 v[66:81], v[142:145], v[102:105], v[66:81]
	ds_read_b128 v[142:145], v204 offset:45056
	v_mfma_f32_32x32x16_bf16 v[66:81], v[172:175], v[98:101], v[66:81]
	ds_read_b128 v[172:175], v212 offset:45056
	s_waitcnt lgkmcnt(3)
	v_mfma_f32_32x32x16_bf16 v[66:81], v[180:183], v[176:179], v[66:81]
	ds_read_b128 v[180:183], v220 offset:45056
	v_mfma_f32_32x32x16_bf16 v[66:81], v[188:191], v[184:187], v[66:81]
	ds_read_b128 v[188:191], v196 offset:45184
	v_mfma_f32_32x32x16_bf16 v[66:81], v[200:203], v[192:195], v[66:81]
	ds_read_b128 v[200:203], v204 offset:45184
	v_mfma_f32_32x32x16_bf16 v[66:81], v[216:219], v[208:211], v[66:81]
	ds_read_b128 v[216:219], v212 offset:45184
	s_waitcnt lgkmcnt(3)
	v_mfma_f32_32x32x16_bf16 v[82:97], v[138:141], v[126:129], 0
	ds_read_b128 v[138:141], v220 offset:45184
	s_add_i32 s78, s78, 2
	s_min_u32 s6, s78, s14
	s_lshl_b32 s7, s6, 6
	s_cmp_lt_u32 s6, 4
	s_cselect_b32 s6, s74, s15
	s_add_i32 s6, s6, s7
	s_mul_hi_i32 s7, s6, 0x1080
	v_mfma_f32_32x32x16_bf16 v[82:97], v[142:145], v[122:125], v[82:97]
	ds_read_b128 v[196:199], v196 offset:45312
	s_mulk_i32 s6, 0x1080
	v_mfma_f32_32x32x16_bf16 v[82:97], v[172:175], v[118:121], v[82:97]
	ds_read_b128 v[204:207], v204 offset:45312
	v_mfma_f32_32x32x16_bf16 v[82:97], v[180:183], v[114:117], v[82:97]
	ds_read_b128 v[212:215], v212 offset:45312
	s_waitcnt lgkmcnt(3)
	v_mfma_f32_32x32x16_bf16 v[82:97], v[188:191], v[110:113], v[82:97]
	ds_read_b128 v[220:223], v220 offset:45312
	s_add_u32 s6, s3, s6
	s_addc_u32 s7, s35, s7
	s_add_i32 s12, s12, s30
	v_mfma_f32_32x32x16_bf16 v[82:97], v[200:203], v[106:109], v[82:97]
	s_add_i32 s12, s12, s8
	s_add_i32 m0, s12, 0x20000
	s_nop 0
	global_load_lds_dwordx4 v232, s[6:7]
	v_mfma_f32_32x32x16_bf16 v[82:97], v[216:219], v[102:105], v[82:97]
	s_add_i32 m0, s12, 0x20400
	v_mfma_f32_32x32x16_bf16 v[82:97], v[138:141], v[98:101], v[82:97]
	global_load_lds_dwordx4 v251, s[6:7]
	s_add_i32 m0, s12, 0x20800
	s_waitcnt lgkmcnt(0)
	v_mfma_f32_32x32x16_bf16 v[82:97], v[196:199], v[176:179], v[82:97]
	v_mfma_f32_32x32x16_bf16 v[82:97], v[204:207], v[184:187], v[82:97]
	global_load_lds_dwordx4 v252, s[6:7]
	v_mfma_f32_32x32x16_bf16 v[82:97], v[212:215], v[192:195], v[82:97]
	v_mfma_f32_32x32x16_bf16 v[82:97], v[220:223], v[208:211], v[82:97]
	v_add_f32_e32 v138, 0, v171
	v_add_f32_e32 v138, v237, v138
	v_add_f32_e32 v138, v224, v138
	v_add_f32_e32 v138, v238, v138
	v_add_f32_e32 v138, v225, v138
	v_add_f32_e32 v138, v239, v138
	v_add_f32_e32 v138, v226, v138
	v_add_f32_e32 v138, v240, v138
	v_add_f32_e32 v138, v227, v138
	v_add_f32_e32 v138, v241, v138
	v_add_f32_e32 v138, v228, v138
	v_add_f32_e32 v138, v242, v138
	v_exp_f32_e32 v132, v132
	v_add_f32_e32 v138, v229, v138
	v_exp_f32_e32 v172, v231
	v_add_f32_e32 v138, v243, v138
	v_exp_f32_e32 v133, v133
	v_add_f32_e32 v138, v230, v138
	v_exp_f32_e32 v173, v233
	v_add_f32_e32 v138, v244, v138
	v_exp_f32_e32 v146, v146
	v_add_f32_e32 v138, v132, v138
	v_exp_f32_e32 v174, v234
	v_add_f32_e32 v138, v172, v138
	v_exp_f32_e32 v147, v147
	v_add_f32_e32 v138, v133, v138
	v_exp_f32_e32 v175, v235
	v_add_f32_e32 v138, v173, v138
	v_exp_f32_e32 v165, v165
	v_add_f32_e32 v138, v146, v138
	v_exp_f32_e32 v176, v236
	v_add_f32_e32 v138, v174, v138
	v_exp_f32_e32 v166, v166
	v_add_f32_e32 v138, v147, v138
	v_exp_f32_e32 v177, v245
	v_add_f32_e32 v138, v175, v138
	v_exp_f32_e32 v168, v168
	v_add_f32_e32 v138, v165, v138
	v_exp_f32_e32 v178, v246
	v_add_f32_e32 v138, v176, v138
	v_exp_f32_e32 v169, v169
	v_add_f32_e32 v138, v166, v138
	v_exp_f32_e32 v131, v131
	v_add_f32_e32 v138, v177, v138
	v_add_f32_e32 v138, v168, v138
	v_add_f32_e32 v138, v178, v138
	v_add_f32_e32 v138, v169, v138
	v_add_f32_e32 v185, v131, v138
	v_mov_b32_e32 v186, v185
	s_nop 1
	v_permlane32_swap_b32_e32 v185, v186
	v_cvt_pk_bf16_f32 v138, v171, v237
	v_cvt_pk_bf16_f32 v139, v224, v238
	v_cvt_pk_bf16_f32 v140, v225, v239
	v_cvt_pk_bf16_f32 v141, v226, v240
	v_cvt_pk_bf16_f32 v142, v227, v241
	v_cvt_pk_bf16_f32 v143, v228, v242
	v_cvt_pk_bf16_f32 v144, v229, v243
	v_cvt_pk_bf16_f32 v145, v230, v244
	v_cvt_pk_bf16_f32 v172, v132, v172
	v_cvt_pk_bf16_f32 v173, v133, v173
	v_cvt_pk_bf16_f32 v174, v146, v174
	v_cvt_pk_bf16_f32 v175, v147, v175
	v_cvt_pk_bf16_f32 v176, v165, v176
	v_cvt_pk_bf16_f32 v177, v166, v177
	v_cvt_pk_bf16_f32 v178, v168, v178
	v_cvt_pk_bf16_f32 v179, v169, v131
	s_nop 0
	v_permlane32_swap_b32_e32 v138, v140
	v_permlane32_swap_b32_e32 v139, v141
	v_permlane32_swap_b32_e32 v142, v144
	v_permlane32_swap_b32_e32 v143, v145
	v_permlane32_swap_b32_e32 v172, v174
	v_permlane32_swap_b32_e32 v173, v175
	v_permlane32_swap_b32_e32 v176, v178
	v_permlane32_swap_b32_e32 v177, v179
	ds_read_b64_tr_b16 v[180:181], v156 offset:0
	ds_read_b64_tr_b16 v[182:183], v156 offset:0x800
	ds_read_b64_tr_b16 v[188:189], v156 offset:0x1000
	ds_read_b64_tr_b16 v[190:191], v156 offset:0x1800
	ds_read_b64_tr_b16 v[192:193], v156 offset:0x2000
	ds_read_b64_tr_b16 v[194:195], v156 offset:0x2800
	ds_read_b64_tr_b16 v[196:197], v156 offset:0x3000
	ds_read_b64_tr_b16 v[198:199], v156 offset:0x3800
	s_nop 0
	s_waitcnt lgkmcnt(6)
	v_mfma_f32_32x32x16_bf16 v[2:17], v[138:141], v[180:183], v[2:17]
	ds_read_b64_tr_b16 v[180:181], v156 offset:0x200
	ds_read_b64_tr_b16 v[182:183], v156 offset:0xa00
	s_waitcnt lgkmcnt(6)
	v_mfma_f32_32x32x16_bf16 v[2:17], v[142:145], v[188:191], v[2:17]
	ds_read_b64_tr_b16 v[188:189], v156 offset:0x1200
	ds_read_b64_tr_b16 v[190:191], v156 offset:0x1a00
	s_waitcnt lgkmcnt(6)
	v_mfma_f32_32x32x16_bf16 v[2:17], v[172:175], v[192:195], v[2:17]
	ds_read_b64_tr_b16 v[192:193], v156 offset:0x2200
	ds_read_b64_tr_b16 v[194:195], v156 offset:0x2a00
	ds_read_b64_tr_b16 v[200:201], v156 offset:0x3200
	ds_read_b64_tr_b16 v[202:203], v156 offset:0x3a00
	s_waitcnt lgkmcnt(8)
	v_mfma_f32_32x32x16_bf16 v[2:17], v[176:179], v[196:199], v[2:17]
	s_waitcnt lgkmcnt(6)
	v_mfma_f32_32x32x16_bf16 v[50:65], v[138:141], v[180:183], v[50:65]
	ds_read_b64_tr_b16 v[180:181], v156 offset:0x400
	ds_read_b64_tr_b16 v[182:183], v156 offset:0xc00
	s_waitcnt lgkmcnt(6)
	v_mfma_f32_32x32x16_bf16 v[50:65], v[142:145], v[188:191], v[50:65]
	ds_read_b64_tr_b16 v[188:189], v156 offset:0x1400
	ds_read_b64_tr_b16 v[190:191], v156 offset:0x1c00
	s_waitcnt lgkmcnt(6)
	v_mfma_f32_32x32x16_bf16 v[50:65], v[172:175], v[192:195], v[50:65]
	ds_read_b64_tr_b16 v[192:193], v156 offset:0x2400
	ds_read_b64_tr_b16 v[194:195], v156 offset:0x2c00
	ds_read_b64_tr_b16 v[196:197], v156 offset:0x3400
	ds_read_b64_tr_b16 v[198:199], v156 offset:0x3c00
	s_waitcnt lgkmcnt(8)
	v_mfma_f32_32x32x16_bf16 v[50:65], v[176:179], v[200:203], v[50:65]
	s_waitcnt lgkmcnt(6)
	v_mfma_f32_32x32x16_bf16 v[34:49], v[138:141], v[180:183], v[34:49]
	ds_read_b64_tr_b16 v[180:181], v156 offset:0x600
	ds_read_b64_tr_b16 v[182:183], v156 offset:0xe00
	s_waitcnt lgkmcnt(6)
	v_mfma_f32_32x32x16_bf16 v[34:49], v[142:145], v[188:191], v[34:49]
	ds_read_b64_tr_b16 v[188:189], v156 offset:0x1600
	ds_read_b64_tr_b16 v[190:191], v156 offset:0x1e00
	s_waitcnt lgkmcnt(6)
	v_mfma_f32_32x32x16_bf16 v[34:49], v[172:175], v[192:195], v[34:49]
	ds_read_b64_tr_b16 v[192:193], v156 offset:0x2600
	ds_read_b64_tr_b16 v[194:195], v156 offset:0x2e00
	ds_read_b64_tr_b16 v[200:201], v156 offset:0x3600
	ds_read_b64_tr_b16 v[202:203], v156 offset:0x3e00
	s_waitcnt lgkmcnt(8)
	v_mfma_f32_32x32x16_bf16 v[34:49], v[176:179], v[196:199], v[34:49]
	s_waitcnt vmcnt(3) lgkmcnt(0)
	s_barrier
	v_mfma_f32_32x32x16_bf16 v[18:33], v[138:141], v[180:183], v[18:33]
	s_mov_b32 m0, s76
	s_nop 0
	global_load_lds_dwordx4 v253, s[10:11]
	s_mov_b32 m0, s77
	v_max_f32_e32 v132, v66, v66
	global_load_lds_dwordx4 v254, s[10:11]
	v_max_f32_e32 v131, v67, v67
	v_max_f32_e32 v131, v132, v131
	v_max3_f32 v131, v131, v68, v69
	v_max3_f32 v131, v131, v70, v71
	v_max3_f32 v131, v131, v72, v73
	v_max3_f32 v131, v131, v74, v75
	v_mfma_f32_32x32x16_bf16 v[18:33], v[142:145], v[188:191], v[18:33]
	v_max3_f32 v131, v131, v76, v77
	v_max3_f32 v131, v131, v78, v79
	v_max3_f32 v131, v131, v80, v81
	v_max3_f32 v131, v131, v82, v83
	v_max3_f32 v131, v131, v84, v85
	v_max3_f32 v131, v131, v86, v87
	v_max3_f32 v131, v131, v88, v89
	v_max3_f32 v131, v131, v90, v91
	v_mfma_f32_32x32x16_bf16 v[18:33], v[172:175], v[192:195], v[18:33]
	v_max3_f32 v131, v131, v92, v93
	v_max3_f32 v131, v131, v94, v95
	v_max3_f32 v131, v131, v96, v97
	v_mov_b32_e32 v132, v131
	s_nop 1
	v_permlane32_swap_b32_e32 v131, v132
	v_max_f32_e32 v132, v132, v132
	v_max_f32_e32 v131, v131, v131
	v_max_f32_e32 v131, v131, v132
	v_max_f32_e32 v133, v130, v130
	v_sub_f32_e32 v132, v131, v130
	v_max_f32_e32 v131, v133, v131
	v_mfma_f32_32x32x16_bf16 v[18:33], v[176:179], v[200:203], v[18:33]
	v_sub_f32_e32 v133, v130, v131
	v_mul_f32_e32 v133, 0x3dd53b94, v133
	v_exp_f32_e32 v133, v133
	v_cmp_ge_f32_e32 vcc, s65, v132
	s_cmp_eq_u64 vcc, exec
	s_cselect_b64 s[6:7], -1, 0
	v_cndmask_b32_e64 v166, v133, 1.0, s[6:7]
	v_cmp_gt_f32_e32 vcc, 1.0, v166
	s_cbranch_vccz .LBB0_1181
	s_and_saveexec_b64 s[10:11], s[4:5]
	ds_write_b32 v155, v166 offset:128
	s_or_b64 exec, exec, s[10:11]
	s_waitcnt lgkmcnt(0)
	v_add_u32_e32 v132, s69, v134
	ds_read_b128 v[138:141], v132 offset:224
	ds_read_b128 v[142:145], v132 offset:192
	ds_read_b128 v[172:175], v132 offset:160
	ds_read_b128 v[176:179], v132 offset:128
	s_waitcnt lgkmcnt(0)
	v_pk_mul_f32 v[14:15], v[14:15], v[138:139]
	v_pk_mul_f32 v[10:11], v[10:11], v[142:143]
	v_pk_mul_f32 v[6:7], v[6:7], v[172:173]
	v_pk_mul_f32 v[16:17], v[16:17], v[140:141]
	v_pk_mul_f32 v[12:13], v[12:13], v[144:145]
	v_pk_mul_f32 v[8:9], v[8:9], v[174:175]
	v_pk_mul_f32 v[4:5], v[4:5], v[178:179]
	v_pk_mul_f32 v[2:3], v[2:3], v[176:177]
	v_pk_mul_f32 v[62:63], v[62:63], v[138:139]
	v_pk_mul_f32 v[58:59], v[58:59], v[142:143]
	v_pk_mul_f32 v[54:55], v[54:55], v[172:173]
	v_pk_mul_f32 v[64:65], v[64:65], v[140:141]
	v_pk_mul_f32 v[60:61], v[60:61], v[144:145]
	v_pk_mul_f32 v[56:57], v[56:57], v[174:175]
	v_pk_mul_f32 v[52:53], v[52:53], v[178:179]
	v_pk_mul_f32 v[50:51], v[50:51], v[176:177]
	v_pk_mul_f32 v[46:47], v[46:47], v[138:139]
	v_pk_mul_f32 v[42:43], v[42:43], v[142:143]
	v_pk_mul_f32 v[38:39], v[38:39], v[172:173]
	v_pk_mul_f32 v[48:49], v[48:49], v[140:141]
	v_pk_mul_f32 v[44:45], v[44:45], v[144:145]
	v_pk_mul_f32 v[40:41], v[40:41], v[174:175]
	v_pk_mul_f32 v[36:37], v[36:37], v[178:179]
	v_pk_mul_f32 v[34:35], v[34:35], v[176:177]
	v_pk_mul_f32 v[30:31], v[30:31], v[138:139]
	v_pk_mul_f32 v[26:27], v[26:27], v[142:143]
	v_pk_mul_f32 v[22:23], v[22:23], v[172:173]
	v_pk_mul_f32 v[32:33], v[32:33], v[140:141]
	v_pk_mul_f32 v[28:29], v[28:29], v[144:145]
	v_pk_mul_f32 v[24:25], v[24:25], v[174:175]
	v_pk_mul_f32 v[20:21], v[20:21], v[178:179]
	v_pk_mul_f32 v[18:19], v[18:19], v[176:177]
